# P6 ln_router: loop-invariant router-bias load hoisted out of the 16-row group loop (was an exposed load -> vmcnt(0) after a barrier every group)
# speedup vs baseline: 1.0003x; 1.0003x over previous
.LBB0_980:
	s_lshl_b32 s14, s56, 10
	s_mov_b32 s57, s15
	s_lshl_b64 s[10:11], s[56:57], 25
	s_lshl_b64 s[20:21], s[14:15], 2
	s_add_u32 s22, s4, s20
	s_addc_u32 s23, s5, s21
	s_add_u32 s6, s6, s20
	s_addc_u32 s7, s7, s21
	v_lshrrev_b32_e32 v103, 4, v100
	s_add_u32 s10, s18, s10
	v_lshlrev_b32_e32 v34, 3, v103
	s_addc_u32 s11, s19, s11
	v_lshl_or_b32 v82, s30, 7, v34
	s_add_u32 s4, s10, 0x4400000
	v_ashrrev_i32_e32 v83, 31, v82
	s_addc_u32 s5, s11, 0
	v_lshlrev_b64 v[34:35], 1, v[82:83]
	v_or_b32_e32 v52, 32, v82
	v_or_b32_e32 v66, 64, v82
	v_or_b32_e32 v82, 0x60, v82
	s_add_u32 s10, s10, 0x4410000
	v_and_b32_e32 v102, 15, v224
	v_lshlrev_b64 v[194:195], 2, v[98:99]
	v_lshlrev_b64 v[196:197], 2, v[98:99]
	v_ashrrev_i32_e32 v53, 31, v52
	v_ashrrev_i32_e32 v67, 31, v66
	v_ashrrev_i32_e32 v83, 31, v82
	s_addc_u32 s11, s11, 0
	v_lshl_add_u64 v[2:3], s[22:23], 0, v[194:195]
	v_lshl_add_u64 v[6:7], s[6:7], 0, v[194:195]
	v_lshl_add_u64 v[26:27], s[22:23], 0, v[196:197]
	v_lshlrev_b32_e32 v50, 11, v102
	v_mov_b32_e32 v51, v1
	v_lshlrev_b64 v[52:53], 1, v[52:53]
	v_lshlrev_b64 v[66:67], 1, v[66:67]
	v_lshlrev_b64 v[82:83], 1, v[82:83]
	global_load_dwordx4 v[2:5], v[2:3], off
	v_lshl_add_u64 v[30:31], s[6:7], 0, v[196:197]
	global_load_dwordx4 v[6:9], v[6:7], off
	s_nop 0
	global_load_dwordx4 v[10:13], v[26:27], off offset:1024
	global_load_dwordx4 v[14:17], v[26:27], off offset:2048
	global_load_dwordx4 v[18:21], v[30:31], off offset:1024
	global_load_dwordx4 v[22:25], v[30:31], off offset:2048
	v_lshl_add_u64 v[42:43], s[4:5], 0, v[34:35]
	v_lshl_add_u64 v[44:45], s[10:11], 0, v[34:35]
	v_or_b32_e32 v90, 0x8000, v50
	v_mov_b32_e32 v91, v1
	v_lshl_add_u64 v[58:59], s[4:5], 0, v[52:53]
	v_lshl_add_u64 v[60:61], s[10:11], 0, v[52:53]
	v_lshl_add_u64 v[84:85], s[4:5], 0, v[50:51]
	v_lshl_add_u64 v[86:87], s[10:11], 0, v[50:51]
	v_lshl_add_u64 v[74:75], s[4:5], 0, v[66:67]
	v_lshl_add_u64 v[76:77], s[10:11], 0, v[66:67]
	v_lshl_add_u64 v[92:93], s[4:5], 0, v[82:83]
	v_lshl_add_u64 v[94:95], s[10:11], 0, v[82:83]
	v_lshl_add_u64 v[34:35], v[42:43], 0, v[50:51]
	v_lshl_add_u64 v[38:39], v[44:45], 0, v[50:51]
	v_lshl_add_u64 v[42:43], v[42:43], 0, v[90:91]
	v_lshl_add_u64 v[46:47], v[44:45], 0, v[90:91]
	v_lshl_add_u64 v[54:55], v[84:85], 0, v[52:53]
	v_lshl_add_u64 v[56:57], v[86:87], 0, v[52:53]
	v_lshl_add_u64 v[58:59], v[58:59], 0, v[90:91]
	v_lshl_add_u64 v[62:63], v[60:61], 0, v[90:91]
	v_lshl_add_u64 v[68:69], v[84:85], 0, v[66:67]
	v_lshl_add_u64 v[70:71], v[86:87], 0, v[66:67]
	v_lshl_add_u64 v[74:75], v[74:75], 0, v[90:91]
	v_lshl_add_u64 v[78:79], v[76:77], 0, v[90:91]
	v_lshl_add_u64 v[84:85], v[84:85], 0, v[82:83]
	v_lshl_add_u64 v[86:87], v[86:87], 0, v[82:83]
	v_lshl_add_u64 v[92:93], v[92:93], 0, v[90:91]
	v_lshl_add_u64 v[94:95], v[94:95], 0, v[90:91]
	global_load_dwordx4 v[26:29], v[26:27], off offset:3072
	s_nop 0
	global_load_dwordx4 v[30:33], v[30:31], off offset:3072
	s_nop 0
	global_load_dwordx4 v[34:37], v[34:35], off
	s_nop 0
	global_load_dwordx4 v[38:41], v[38:39], off
	s_nop 0
	global_load_dwordx4 v[42:45], v[42:43], off
	s_nop 0
	global_load_dwordx4 v[46:49], v[46:47], off
	s_nop 0
	global_load_dwordx4 v[50:53], v[54:55], off
	s_nop 0
	global_load_dwordx4 v[54:57], v[56:57], off
	s_nop 0
	global_load_dwordx4 v[58:61], v[58:59], off
	s_nop 0
	global_load_dwordx4 v[62:65], v[62:63], off
	s_nop 0
	global_load_dwordx4 v[66:69], v[68:69], off
	s_nop 0
	global_load_dwordx4 v[70:73], v[70:71], off
	s_nop 0
	global_load_dwordx4 v[74:77], v[74:75], off
	s_nop 0
	global_load_dwordx4 v[78:81], v[78:79], off
	s_nop 0
	global_load_dwordx4 v[82:85], v[84:85], off
	s_nop 0
	global_load_dwordx4 v[86:89], v[86:87], off
	s_nop 0
	global_load_dwordx4 v[90:93], v[92:93], off
	s_nop 0
	global_load_dwordx4 v[94:97], v[94:95], off
	v_and_b32_e32 v104, 64, v213
	v_add_u32_e32 v104, 64, v104
	v_xor_b32_e32 v105, 1, v213
	v_cmp_lt_i32_e32 vcc, v105, v104
	s_lshl_b32 s14, s56, 5
	s_add_u32 s20, s18, 0x12900000
	v_cndmask_b32_e32 v105, v213, v105, vcc
	v_lshlrev_b32_e32 v226, 2, v105
	v_xor_b32_e32 v105, 2, v213
	v_cmp_lt_i32_e32 vcc, v105, v104
	s_mul_i32 s4, s56, 0x36000
	s_addc_u32 s21, s19, 0
	v_cndmask_b32_e32 v105, v213, v105, vcc
	v_lshlrev_b32_e32 v227, 2, v105
	v_xor_b32_e32 v105, 4, v213
	s_add_u32 s4, s18, s4
	v_cmp_lt_i32_e32 vcc, v105, v104
	s_addc_u32 s5, s19, 0
	s_add_u32 s44, s4, 0x100000
	v_cndmask_b32_e32 v105, v213, v105, vcc
	v_lshlrev_b32_e32 v228, 2, v105
	v_xor_b32_e32 v105, 8, v213
	s_addc_u32 s45, s5, 0
	s_lshl_b64 s[4:5], s[14:15], 2
	v_cmp_lt_i32_e32 vcc, v105, v104
	s_add_u32 s34, s8, s4
	s_addc_u32 s35, s9, s5
	v_cndmask_b32_e32 v105, v213, v105, vcc
	v_lshlrev_b32_e32 v229, 2, v105
	v_xor_b32_e32 v105, 16, v213
	s_add_u32 s22, s18, 0x300000
	v_cmp_lt_i32_e32 vcc, v105, v104
	s_addc_u32 s23, s19, 0
	s_add_u32 s24, s18, 0x500000
	v_cndmask_b32_e32 v105, v213, v105, vcc
	v_lshlrev_b32_e32 v230, 2, v105
	v_xor_b32_e32 v105, 32, v213
	s_addc_u32 s25, s19, 0
	v_cmp_lt_i32_e32 vcc, v105, v104
	s_add_u32 s26, s18, 0x700000
	s_movk_i32 s4, 0x810
	v_cndmask_b32_e32 v104, v213, v105, vcc
	v_lshlrev_b32_e32 v103, 9, v103
	s_addc_u32 s27, s19, 0
	s_lshl_b32 s14, s30, 1
	v_lshlrev_b32_e32 v231, 2, v104
	v_and_b32_e32 v104, 48, v224
	v_mad_u32_u24 v105, v102, s4, 0
	v_lshl_or_b32 v106, s30, 11, v103
	v_readlane_b32 s4, v253, 2
	v_and_b32_e32 v103, 0xffffffe0, v224
	v_and_b32_e32 v232, 31, v224
	v_lshl_or_b32 v104, s30, 8, v104
	v_lshl_add_u32 v107, v102, 2, s4
	v_lshlrev_b32_e32 v108, 2, v103
	v_lshlrev_b32_e32 v102, 2, v232
	v_readlane_b32 s29, v253, 3
	s_cmp_lt_u32 s28, 64
	s_mulk_i32 s30, 0x1020
	v_add3_u32 v233, s4, v108, v102
	v_add_u32_e32 v108, s29, v103
	v_lshlrev_b32_e32 v109, 3, v232
	s_cselect_b64 s[28:29], -1, 0
	v_lshlrev_b32_e32 v110, 3, v100
	s_add_i32 s47, s30, 0
	s_or_b32 s30, s14, 1
	v_mov_b32_e32 v103, v1
	v_or_b32_e32 v0, 0x100, v101
	v_or_b32_e32 v198, 0x200, v101
	v_or_b32_e32 v200, 0x300, v101
	s_mulk_i32 s30, 0x810
	v_lshl_add_u64 v[202:203], s[20:21], 0, v[98:99]
	v_lshl_add_u64 v[204:205], s[34:35], 0, v[102:103]
	v_lshl_add_u64 v[206:207], s[12:13], 0, v[194:195]
	v_readlane_b32 s12, v252, 59
	v_add_u32_e32 v238, v105, v104
	v_add_u32_e32 v239, v107, v106
	v_add_u32_e32 v240, v108, v109
	v_add_u32_e32 v98, 0, v110
	s_waitcnt vmcnt(31)
	v_mov_b64_e32 v[102:103], v[190:191]
	s_waitcnt vmcnt(30)
	v_mov_b64_e32 v[106:107], v[186:187]
	s_waitcnt vmcnt(29)
	v_mov_b64_e32 v[110:111], v[182:183]
	s_waitcnt vmcnt(28)
	v_mov_b64_e32 v[114:115], v[178:179]
	s_waitcnt vmcnt(27)
	v_mov_b64_e32 v[122:123], v[174:175]
	s_waitcnt vmcnt(26)
	v_mov_b64_e32 v[126:127], v[170:171]
	s_waitcnt vmcnt(25)
	v_mov_b64_e32 v[130:131], v[166:167]
	s_waitcnt vmcnt(24)
	global_load_dword v242, v[204:205], off
	s_waitcnt vmcnt(0)
	v_mov_b64_e32 v[134:135], v[162:163]
	v_mov_b32_e32 v199, v1
	v_mov_b32_e32 v201, v1
	v_cmp_gt_u32_e64 s[10:11], 4, v232
	v_cmp_eq_u32_e64 s[4:5], 0, v232
	v_cmp_eq_u32_e64 s[6:7], 1, v232
	v_cmp_eq_u32_e64 s[8:9], 2, v232
	v_lshlrev_b32_e32 v234, 1, v101
	v_lshlrev_b32_e32 v235, 1, v0
	v_lshlrev_b32_e32 v236, 1, v198
	v_lshlrev_b32_e32 v237, 1, v200
	s_add_i32 s48, s30, 0
	v_add_u32_e32 v208, s12, v100
	s_mov_b32 s50, -1
	v_add_u32_e32 v241, 0x14200, v98
	s_mov_b32 s12, s82
	v_mov_b64_e32 v[104:105], v[192:193]
	v_mov_b64_e32 v[108:109], v[188:189]
	v_mov_b64_e32 v[112:113], v[184:185]
	v_mov_b64_e32 v[116:117], v[180:181]
	v_mov_b64_e32 v[124:125], v[176:177]
	v_mov_b64_e32 v[128:129], v[172:173]
	v_mov_b64_e32 v[132:133], v[168:169]
	v_mov_b64_e32 v[136:137], v[164:165]
	s_branch .LBB0_982

.LBB0_986:
	v_mov_b32_e32 v246, v191
	v_mov_b32_e32 v247, v192
	v_mov_b32_e32 v248, v190
	v_mov_b32_e32 v249, v193
	v_pk_add_f32 v[246:247], v[246:247], v[248:249]
	v_mov_b32_e32 v248, v187
	v_mov_b32_e32 v249, v188
	v_mov_b32_e32 v216, v186
	v_mov_b32_e32 v217, v189
	v_pk_add_f32 v[216:217], v[248:249], v[216:217]
	v_add_f32_e32 v209, v246, v247
	v_pk_add_f32 v[216:217], v[216:217], v[216:217] op_sel:[0,1] op_sel_hi:[1,0]
	v_add_f32_e32 v246, 0, v209
	v_add_f32_e32 v248, v182, v183
	v_add_f32_e32 v218, v184, v185
	v_mov_b32_e32 v247, v178
	v_mov_b32_e32 v217, v179
	v_mov_b32_e32 v249, v180
	v_mov_b32_e32 v219, v181
	v_pk_add_f32 v[216:217], v[246:247], v[216:217]
	v_pk_add_f32 v[218:219], v[248:249], v[218:219]
	s_mov_b32 s36, 0xf800000
	v_pk_add_f32 v[216:217], v[216:217], v[218:219]
	s_nop 0
	v_add_f32_e32 v209, v216, v217
	ds_bpermute_b32 v216, v226, v209
	s_waitcnt lgkmcnt(0)
	v_add_f32_e32 v209, v209, v216
	ds_bpermute_b32 v216, v227, v209
	s_waitcnt lgkmcnt(0)
	v_add_f32_e32 v209, v209, v216
	ds_bpermute_b32 v216, v228, v209
	s_waitcnt lgkmcnt(0)
	v_add_f32_e32 v209, v209, v216
	ds_bpermute_b32 v216, v229, v209
	s_waitcnt lgkmcnt(0)
	v_add_f32_e32 v209, v209, v216
	ds_bpermute_b32 v216, v230, v209
	s_waitcnt lgkmcnt(0)
	v_add_f32_e32 v209, v209, v216
	ds_bpermute_b32 v216, v231, v209
	s_waitcnt lgkmcnt(0)
	v_add_f32_e32 v209, v209, v216
	v_fmamk_f32 v191, v209, 0xba800000, v191
	v_fmamk_f32 v190, v209, 0xba800000, v190
	v_fmamk_f32 v193, v209, 0xba800000, v193
	v_fmac_f32_e32 v192, 0xba800000, v209
	v_pk_mul_f32 v[216:217], v[192:193], v[192:193]
	v_pk_mul_f32 v[218:219], v[190:191], v[190:191]
	v_fmamk_f32 v187, v209, 0xba800000, v187
	v_fmamk_f32 v186, v209, 0xba800000, v186
	v_fmamk_f32 v189, v209, 0xba800000, v189
	v_pk_mov_b32 v[246:247], v[218:219], v[216:217] op_sel:[1,0]
	v_mov_b32_e32 v219, v217
	v_fmac_f32_e32 v188, 0xba800000, v209
	v_pk_add_f32 v[216:217], v[246:247], v[218:219]
	v_pk_mul_f32 v[218:219], v[188:189], v[188:189]
	v_pk_mul_f32 v[246:247], v[186:187], v[186:187]
	v_fmac_f32_e32 v184, 0xba800000, v209
	v_pk_mov_b32 v[248:249], v[246:247], v[218:219] op_sel:[1,0]
	v_mov_b32_e32 v247, v219
	v_pk_add_f32 v[218:219], v[248:249], v[246:247]
	v_fmamk_f32 v246, v209, 0xba800000, v182
	v_fmamk_f32 v247, v209, 0xba800000, v183
	v_mul_f32_e32 v182, v246, v246
	v_pk_fma_f32 v[182:183], v[246:247], v[246:247], v[182:183] op_sel_hi:[1,1,0]
	v_fmamk_f32 v185, v209, 0xba800000, v185
	v_mul_f32_e32 v182, v184, v184
	v_pk_add_f32 v[216:217], v[216:217], v[216:217] op_sel_hi:[0,1]
	v_pk_add_f32 v[218:219], v[218:219], v[218:219] op_sel_hi:[0,1]
	v_pk_fma_f32 v[248:249], v[184:185], v[184:185], v[182:183] op_sel_hi:[1,1,0]
	v_fmamk_f32 v181, v209, 0xba800000, v181
	v_fmamk_f32 v180, v209, 0xba800000, v180
	v_fmamk_f32 v179, v209, 0xba800000, v179
	v_fmac_f32_e32 v178, 0xba800000, v209
	v_mul_f32_e32 v182, v178, v178
	v_mul_f32_e32 v248, v179, v179
	v_mul_f32_e32 v216, v180, v180
	v_mul_f32_e32 v218, v181, v181
	v_pk_add_f32 v[182:183], v[182:183], v[248:249]
	v_pk_add_f32 v[216:217], v[216:217], v[218:219]
	s_nop 0
	v_pk_add_f32 v[182:183], v[182:183], v[216:217]
	s_nop 0
	v_add_f32_e32 v182, v182, v183
	ds_bpermute_b32 v183, v226, v182
	s_waitcnt lgkmcnt(0)
	v_add_f32_e32 v182, v182, v183
	ds_bpermute_b32 v183, v227, v182
	s_waitcnt lgkmcnt(0)
	v_add_f32_e32 v182, v182, v183
	ds_bpermute_b32 v183, v228, v182
	s_waitcnt lgkmcnt(0)
	v_add_f32_e32 v182, v182, v183
	ds_bpermute_b32 v183, v229, v182
	s_waitcnt lgkmcnt(0)
	v_add_f32_e32 v182, v182, v183
	ds_bpermute_b32 v183, v230, v182
	s_waitcnt lgkmcnt(0)
	v_add_f32_e32 v182, v182, v183
	ds_bpermute_b32 v183, v231, v182
	s_waitcnt lgkmcnt(0)
	v_add_f32_e32 v182, v182, v183
	v_fmamk_f32 v182, v182, 0x3a800000, v211
	v_mul_f32_e32 v183, 0x4f800000, v182
	v_cmp_gt_f32_e32 vcc, s36, v182
	s_nop 1
	v_cndmask_b32_e32 v182, v182, v183, vcc
	v_sqrt_f32_e32 v183, v182
	s_nop 0
	v_add_u32_e32 v209, -1, v183
	v_add_u32_e32 v216, 1, v183
	v_fma_f32 v217, -v209, v183, v182
	v_fma_f32 v218, -v216, v183, v182
	v_cmp_ge_f32_e64 s[12:13], 0, v217
	s_nop 1
	v_cndmask_b32_e64 v183, v183, v209, s[12:13]
	v_cmp_lt_f32_e64 s[12:13], 0, v218
	s_nop 1
	v_cndmask_b32_e64 v183, v183, v216, s[12:13]
	v_mul_f32_e32 v209, 0x37800000, v183
	v_cndmask_b32_e32 v183, v183, v209, vcc
	v_cmp_class_f32_e32 vcc, v182, v212
	s_nop 1
	v_cndmask_b32_e32 v182, v183, v182, vcc
	v_div_scale_f32 v183, s[12:13], v182, v182, 1.0
	v_rcp_f32_e32 v209, v183
	v_readlane_b32 s12, v252, 4
	s_add_i32 s34, s12, s14
	s_ashr_i32 s35, s34, 31
	v_fma_f32 v216, -v183, v209, 1.0
	v_fmac_f32_e32 v209, v216, v209
	v_div_scale_f32 v216, vcc, 1.0, v182, 1.0
	v_mul_f32_e32 v217, v216, v209
	v_fma_f32 v218, -v183, v217, v216
	v_fmac_f32_e32 v217, v218, v209
	v_fma_f32 v183, -v183, v217, v216
	v_div_fmas_f32 v183, v183, v209, v217
	v_div_fixup_f32 v182, v183, v182, 1.0
	v_pk_mul_f32 v[190:191], v[190:191], v[182:183] op_sel_hi:[1,0]
	s_lshl_b64 s[12:13], s[34:35], 10
	s_waitcnt vmcnt(22)
	v_pk_fma_f32 v[190:191], v[2:3], v[190:191], v[6:7]
	v_pk_mul_f32 v[192:193], v[192:193], v[182:183] op_sel_hi:[1,0]
	v_pk_fma_f32 v[190:191], v[98:99], v[190:191], v[118:119]
	s_mov_b32 s35, 0xffff
	v_cvt_pk_bf16_f32 v216, v191, 0
	v_cvt_pk_bf16_f32 v183, v190, 0
	v_lshlrev_b32_e32 v216, 16, v216
	v_lshlrev_b32_e32 v209, 16, v183
	v_sub_f32_e32 v217, v191, v216
	v_and_or_b32 v216, v183, s35, v216
	v_mov_b32_e32 v183, v1
	v_cvt_pk_fp8_f32 v183, v190, v191
	v_pk_fma_f32 v[192:193], v[4:5], v[192:193], v[8:9]
	v_cvt_pk_bf16_f32 v218, v217, 0
	v_pk_fma_f32 v[192:193], v[100:101], v[192:193], v[120:121]
	v_sub_f32_e32 v209, v190, v209
	v_cvt_pk_fp8_f32 v183, v192, v193 op_sel:[0,0,1]
	v_cvt_pk_bf16_f32 v217, v192, 0
	v_cvt_pk_bf16_f32 v248, v193, 0
	v_lshlrev_b32_e32 v219, 16, v217
	v_lshlrev_b32_e32 v248, 16, v248
	v_sub_f32_e32 v219, v192, v219
	v_sub_f32_e32 v249, v193, v248
	v_lshl_add_u64 v[192:193], v[202:203], 0, s[12:13]
	global_store_dword v[192:193], v183, off
	v_add_u32_e32 v183, s47, v234
	v_pk_mul_f32 v[186:187], v[186:187], v[182:183] op_sel_hi:[1,0]
	v_cvt_pk_bf16_f32 v249, v249, 0
	s_waitcnt vmcnt(20)
	v_pk_fma_f32 v[186:187], v[10:11], v[186:187], v[18:19]
	v_cvt_pk_bf16_f32 v209, v209, 0
	v_cvt_pk_bf16_f32 v219, v219, 0
	v_and_or_b32 v217, v217, s35, v248
	v_lshlrev_b32_e32 v190, 16, v218
	v_lshlrev_b32_e32 v191, 16, v249
	v_pk_fma_f32 v[186:187], v[138:139], v[186:187], v[142:143]
	v_and_or_b32 v190, v209, s35, v190
	v_and_or_b32 v191, v219, s35, v191
	ds_write_b64 v183, v[216:217]
	ds_write_b64 v183, v[190:191] offset:33024
	v_pk_mul_f32 v[188:189], v[188:189], v[182:183] op_sel_hi:[1,0]
	v_cvt_pk_bf16_f32 v183, v186, 0
	v_lshlrev_b32_e32 v190, 16, v183
	v_sub_f32_e32 v190, v186, v190
	v_cvt_pk_bf16_f32 v192, v190, 0
	v_cvt_pk_bf16_f32 v190, v187, 0
	v_lshlrev_b32_e32 v190, 16, v190
	v_sub_f32_e32 v191, v187, v190
	v_cvt_pk_bf16_f32 v193, v191, 0
	v_and_or_b32 v190, v183, s35, v190
	v_lshlrev_b32_e32 v183, 16, v193
	v_mov_b32_e32 v193, v1
	v_pk_fma_f32 v[188:189], v[12:13], v[188:189], v[20:21]
	v_cvt_pk_fp8_f32 v193, v186, v187
	v_pk_fma_f32 v[188:189], v[140:141], v[188:189], v[144:145]
	s_add_u32 s12, s20, s12
	v_cvt_pk_bf16_f32 v216, v189, 0
	v_cvt_pk_bf16_f32 v191, v188, 0
	v_lshlrev_b32_e32 v216, 16, v216
	v_lshlrev_b32_e32 v209, 16, v191
	v_sub_f32_e32 v217, v189, v216
	v_cvt_pk_fp8_f32 v193, v188, v189 op_sel:[0,0,1]
	v_sub_f32_e32 v209, v188, v209
	v_cvt_pk_bf16_f32 v217, v217, 0
	v_cvt_pk_bf16_f32 v209, v209, 0
	v_and_or_b32 v186, v192, s35, v183
	v_lshlrev_b32_e32 v183, 16, v217
	s_addc_u32 s13, s21, s13
	v_and_or_b32 v191, v191, s35, v216
	v_and_or_b32 v187, v209, s35, v183
	v_lshl_add_u64 v[188:189], s[12:13], 0, v[0:1]
	v_add_u32_e32 v183, s47, v235
	global_store_dword v[188:189], v193, off
	ds_write_b64 v183, v[190:191]
	ds_write_b64 v183, v[186:187] offset:33024
	v_pk_mul_f32 v[186:187], v[246:247], v[182:183] op_sel_hi:[1,0]
	v_pk_mul_f32 v[184:185], v[184:185], v[182:183] op_sel_hi:[1,0]
	s_waitcnt vmcnt(20)
	v_pk_fma_f32 v[186:187], v[14:15], v[186:187], v[22:23]
	v_pk_fma_f32 v[184:185], v[16:17], v[184:185], v[24:25]
	v_pk_fma_f32 v[186:187], v[150:151], v[186:187], v[146:147]
	v_pk_fma_f32 v[184:185], v[152:153], v[184:185], v[148:149]
	v_cvt_pk_bf16_f32 v183, v186, 0
	v_lshlrev_b32_e32 v188, 16, v183
	v_sub_f32_e32 v188, v186, v188
	v_cvt_pk_bf16_f32 v209, v188, 0
	v_cvt_pk_bf16_f32 v188, v187, 0
	v_lshlrev_b32_e32 v218, 16, v188
	v_sub_f32_e32 v188, v187, v218
	v_cvt_pk_bf16_f32 v246, v184, 0
	v_cvt_pk_bf16_f32 v219, v188, 0
	v_lshlrev_b32_e32 v188, 16, v246
	v_sub_f32_e32 v188, v184, v188
	v_cvt_pk_bf16_f32 v247, v188, 0
	v_mov_b32_e32 v188, v175
	v_mov_b32_e32 v189, v176
	v_mov_b32_e32 v190, v174
	v_mov_b32_e32 v191, v177
	v_pk_add_f32 v[188:189], v[188:189], v[190:191]
	v_mov_b32_e32 v190, v171
	v_mov_b32_e32 v191, v172
	v_mov_b32_e32 v192, v170
	v_mov_b32_e32 v193, v173
	v_pk_add_f32 v[190:191], v[190:191], v[192:193]
	v_add_f32_e32 v188, v188, v189
	v_pk_add_f32 v[190:191], v[190:191], v[190:191] op_sel:[0,1] op_sel_hi:[1,0]
	v_add_f32_e32 v188, 0, v188
	v_add_f32_e32 v192, v166, v167
	v_add_f32_e32 v216, v168, v169
	v_mov_b32_e32 v189, v162
	v_mov_b32_e32 v191, v163
	v_mov_b32_e32 v193, v164
	v_mov_b32_e32 v217, v165
	v_pk_add_f32 v[188:189], v[188:189], v[190:191]
	v_pk_add_f32 v[190:191], v[192:193], v[216:217]
	v_cvt_pk_bf16_f32 v248, v185, 0
	v_pk_add_f32 v[188:189], v[188:189], v[190:191]
	v_lshlrev_b32_e32 v191, 16, v248
	v_add_f32_e32 v189, v188, v189
	ds_bpermute_b32 v190, v226, v189
	v_sub_f32_e32 v188, v185, v191
	v_cvt_pk_bf16_f32 v192, v188, 0
	v_and_or_b32 v188, v183, s35, v218
	v_mov_b32_e32 v193, v1
	s_waitcnt lgkmcnt(0)
	v_add_f32_e32 v183, v189, v190
	ds_bpermute_b32 v190, v227, v183
	v_cvt_pk_fp8_f32 v193, v186, v187
	v_and_or_b32 v189, v246, s35, v191
	v_lshlrev_b32_e32 v191, 16, v219
	v_and_or_b32 v186, v209, s35, v191
	s_waitcnt lgkmcnt(0)
	v_add_f32_e32 v183, v183, v190
	ds_bpermute_b32 v190, v228, v183
	v_cvt_pk_fp8_f32 v193, v184, v185 op_sel:[0,0,1]
	v_lshl_add_u64 v[184:185], s[12:13], 0, v[198:199]
	v_lshlrev_b32_e32 v187, 16, v192
	v_and_or_b32 v187, v247, s35, v187
	s_waitcnt lgkmcnt(0)
	v_add_f32_e32 v183, v183, v190
	ds_bpermute_b32 v190, v229, v183
	global_store_dword v[184:185], v193, off
	v_add_u32_e32 v184, s47, v236
	ds_write_b64 v184, v[188:189]
	ds_write_b64 v184, v[186:187] offset:33024
	s_waitcnt lgkmcnt(2)
	v_add_f32_e32 v183, v183, v190
	ds_bpermute_b32 v185, v230, v183
	v_pk_mul_f32 v[180:181], v[180:181], v[182:183] op_sel_hi:[1,0]
	v_pk_mul_f32 v[178:179], v[178:179], v[182:183] op_sel_hi:[1,0]
	s_waitcnt vmcnt(19)
	v_pk_fma_f32 v[180:181], v[28:29], v[180:181], v[32:33]
	v_pk_fma_f32 v[178:179], v[26:27], v[178:179], v[30:31]
	s_waitcnt lgkmcnt(0)
	v_add_f32_e32 v182, v183, v185
	ds_bpermute_b32 v183, v231, v182
	s_waitcnt vmcnt(3)
	v_pk_fma_f32 v[180:181], v[156:157], v[180:181], v[160:161]
	v_pk_fma_f32 v[178:179], v[154:155], v[178:179], v[158:159]
	s_waitcnt lgkmcnt(0)
	v_add_f32_e32 v191, v182, v183
	v_fmamk_f32 v175, v191, 0xba800000, v175
	v_fmamk_f32 v174, v191, 0xba800000, v174
	v_fmamk_f32 v177, v191, 0xba800000, v177
	v_fmac_f32_e32 v176, 0xba800000, v191
	v_pk_mul_f32 v[182:183], v[176:177], v[176:177]
	v_pk_mul_f32 v[184:185], v[174:175], v[174:175]
	v_fmamk_f32 v171, v191, 0xba800000, v171
	v_pk_mov_b32 v[186:187], v[184:185], v[182:183] op_sel:[1,0]
	v_mov_b32_e32 v185, v183
	v_pk_add_f32 v[182:183], v[186:187], v[184:185]
	v_fmamk_f32 v170, v191, 0xba800000, v170
	v_fmamk_f32 v173, v191, 0xba800000, v173
	v_fmac_f32_e32 v172, 0xba800000, v191
	v_pk_add_f32 v[182:183], v[182:183], v[182:183] op_sel_hi:[0,1]
	v_pk_mul_f32 v[184:185], v[172:173], v[172:173]
	v_pk_mul_f32 v[186:187], v[170:171], v[170:171]
	v_fmamk_f32 v166, v191, 0xba800000, v166
	v_pk_mov_b32 v[188:189], v[186:187], v[184:185] op_sel:[1,0]
	v_mov_b32_e32 v187, v185
	v_fmamk_f32 v167, v191, 0xba800000, v167
	v_fmac_f32_e32 v168, 0xba800000, v191
	v_mul_f32_e32 v182, v166, v166
	v_pk_add_f32 v[184:185], v[188:189], v[186:187]
	v_fmamk_f32 v169, v191, 0xba800000, v169
	v_pk_fma_f32 v[186:187], v[166:167], v[166:167], v[182:183] op_sel_hi:[1,1,0]
	v_mul_f32_e32 v182, v168, v168
	v_pk_add_f32 v[184:185], v[184:185], v[184:185] op_sel_hi:[0,1]
	v_pk_fma_f32 v[188:189], v[168:169], v[168:169], v[182:183] op_sel_hi:[1,1,0]
	v_fmamk_f32 v165, v191, 0xba800000, v165
	v_fmamk_f32 v164, v191, 0xba800000, v164
	v_fmamk_f32 v163, v191, 0xba800000, v163
	v_fmac_f32_e32 v162, 0xba800000, v191
	v_mul_f32_e32 v186, v162, v162
	v_mul_f32_e32 v188, v163, v163
	v_mul_f32_e32 v182, v164, v164
	v_mul_f32_e32 v184, v165, v165
	v_pk_add_f32 v[186:187], v[186:187], v[188:189]
	v_pk_add_f32 v[182:183], v[182:183], v[184:185]
	v_cvt_pk_bf16_f32 v189, v181, 0
	v_pk_add_f32 v[182:183], v[186:187], v[182:183]
	v_cvt_pk_bf16_f32 v185, v179, 0
	v_add_f32_e32 v182, v182, v183
	ds_bpermute_b32 v183, v226, v182
	v_lshlrev_b32_e32 v189, 16, v189
	v_cvt_pk_bf16_f32 v190, v178, 0
	v_lshlrev_b32_e32 v185, 16, v185
	v_sub_f32_e32 v186, v179, v185
	s_waitcnt lgkmcnt(0)
	v_add_f32_e32 v182, v182, v183
	ds_bpermute_b32 v183, v227, v182
	v_lshlrev_b32_e32 v184, 16, v190
	v_cvt_pk_bf16_f32 v187, v180, 0
	v_lshlrev_b32_e32 v188, 16, v187
	v_sub_f32_e32 v188, v180, v188
	s_waitcnt lgkmcnt(0)
	v_add_f32_e32 v182, v182, v183
	ds_bpermute_b32 v183, v228, v182
	v_sub_f32_e32 v184, v178, v184
	v_cvt_pk_bf16_f32 v186, v186, 0
	v_cvt_pk_bf16_f32 v184, v184, 0
	v_lshlrev_b32_e32 v186, 16, v186
	s_waitcnt lgkmcnt(0)
	v_add_f32_e32 v183, v182, v183
	ds_bpermute_b32 v191, v229, v183
	v_sub_f32_e32 v182, v181, v189
	v_cvt_pk_bf16_f32 v192, v182, 0
	v_and_or_b32 v182, v190, s35, v185
	v_cvt_pk_bf16_f32 v188, v188, 0
	s_waitcnt lgkmcnt(0)
	v_add_f32_e32 v185, v183, v191
	ds_bpermute_b32 v190, v230, v185
	v_and_or_b32 v183, v187, s35, v189
	v_mov_b32_e32 v187, v1
	v_cvt_pk_fp8_f32 v187, v178, v179
	v_and_or_b32 v178, v184, s35, v186
	s_waitcnt lgkmcnt(0)
	v_add_f32_e32 v185, v185, v190
	ds_bpermute_b32 v189, v231, v185
	v_cvt_pk_fp8_f32 v187, v180, v181 op_sel:[0,0,1]
	v_lshlrev_b32_e32 v179, 16, v192
	v_and_or_b32 v179, v188, s35, v179
	s_waitcnt lgkmcnt(0)
	v_add_f32_e32 v180, v185, v189
	v_fmamk_f32 v180, v180, 0x3a800000, v211
	v_mul_f32_e32 v181, 0x4f800000, v180
	v_cmp_gt_f32_e32 vcc, s36, v180
	s_nop 1
	v_cndmask_b32_e32 v184, v180, v181, vcc
	v_sqrt_f32_e32 v185, v184
	v_lshl_add_u64 v[180:181], s[12:13], 0, v[200:201]
	global_store_dword v[180:181], v187, off
	v_add_u32_e32 v180, s47, v237
	v_add_u32_e32 v181, -1, v185
	v_fma_f32 v186, -v181, v185, v184
	v_cmp_ge_f32_e64 s[12:13], 0, v186
	v_add_u32_e32 v186, 1, v185
	ds_write_b64 v180, v[182:183]
	ds_write_b64 v180, v[178:179] offset:33024
	v_cndmask_b32_e64 v181, v185, v181, s[12:13]
	v_fma_f32 v185, -v186, v185, v184
	v_cmp_lt_f32_e64 s[12:13], 0, v185
	s_nop 1
	v_cndmask_b32_e64 v181, v181, v186, s[12:13]
	v_mul_f32_e32 v185, 0x37800000, v181
	v_cndmask_b32_e32 v181, v181, v185, vcc
	v_cmp_class_f32_e32 vcc, v184, v212
	s_nop 1
	v_cndmask_b32_e32 v181, v181, v184, vcc
	v_div_scale_f32 v184, s[12:13], v181, v181, 1.0
	v_rcp_f32_e32 v185, v184
	s_add_i32 s12, s34, 1
	s_ashr_i32 s13, s12, 31
	s_lshl_b64 s[12:13], s[12:13], 10
	v_fma_f32 v178, -v184, v185, 1.0
	v_fmac_f32_e32 v185, v178, v185
	v_div_scale_f32 v178, vcc, 1.0, v181, 1.0
	v_mul_f32_e32 v179, v178, v185
	v_fma_f32 v180, -v184, v179, v178
	v_fmac_f32_e32 v179, v180, v185
	v_fma_f32 v178, -v184, v179, v178
	v_div_fmas_f32 v178, v178, v185, v179
	v_div_fixup_f32 v178, v178, v181, 1.0
	v_pk_mul_f32 v[174:175], v[174:175], v[178:179] op_sel_hi:[1,0]
	v_pk_mul_f32 v[176:177], v[176:177], v[178:179] op_sel_hi:[1,0]
	v_pk_fma_f32 v[174:175], v[2:3], v[174:175], v[6:7]
	v_pk_fma_f32 v[176:177], v[4:5], v[176:177], v[8:9]
	v_pk_fma_f32 v[174:175], v[98:99], v[174:175], v[118:119]
	v_pk_fma_f32 v[176:177], v[100:101], v[176:177], v[120:121]
	v_cvt_pk_bf16_f32 v179, v174, 0
	v_lshlrev_b32_e32 v180, 16, v179
	v_sub_f32_e32 v180, v174, v180
	v_cvt_pk_bf16_f32 v182, v180, 0
	v_cvt_pk_bf16_f32 v180, v175, 0
	v_lshlrev_b32_e32 v180, 16, v180
	v_sub_f32_e32 v181, v175, v180
	v_and_or_b32 v180, v179, s35, v180
	v_mov_b32_e32 v179, v1
	v_cvt_pk_fp8_f32 v179, v174, v175
	v_cvt_pk_bf16_f32 v185, v177, 0
	v_cvt_pk_bf16_f32 v183, v181, 0
	v_cvt_pk_bf16_f32 v181, v176, 0
	v_cvt_pk_fp8_f32 v179, v176, v177 op_sel:[0,0,1]
	v_lshlrev_b32_e32 v185, 16, v185
	v_lshlrev_b32_e32 v184, 16, v181
	v_sub_f32_e32 v186, v177, v185
	v_pk_mul_f32 v[170:171], v[170:171], v[178:179] op_sel_hi:[1,0]
	v_sub_f32_e32 v184, v176, v184
	v_cvt_pk_bf16_f32 v186, v186, 0
	v_lshlrev_b32_e32 v174, 16, v183
	v_lshl_add_u64 v[176:177], v[202:203], 0, s[12:13]
	v_pk_fma_f32 v[170:171], v[10:11], v[170:171], v[18:19]
	v_cvt_pk_bf16_f32 v184, v184, 0
	v_and_or_b32 v181, v181, s35, v185
	v_and_or_b32 v174, v182, s35, v174
	v_lshlrev_b32_e32 v175, 16, v186
	global_store_dword v[176:177], v179, off
	v_add_u32_e32 v176, s48, v234
	v_pk_fma_f32 v[170:171], v[138:139], v[170:171], v[142:143]
	v_and_or_b32 v175, v184, s35, v175
	ds_write_b64 v176, v[180:181]
	ds_write_b64 v176, v[174:175] offset:33024
	v_pk_mul_f32 v[172:173], v[172:173], v[178:179] op_sel_hi:[1,0]
	v_cvt_pk_bf16_f32 v174, v170, 0
	v_pk_fma_f32 v[172:173], v[12:13], v[172:173], v[20:21]
	v_lshlrev_b32_e32 v175, 16, v174
	v_pk_fma_f32 v[172:173], v[140:141], v[172:173], v[144:145]
	v_sub_f32_e32 v175, v170, v175
	v_cvt_pk_bf16_f32 v176, v175, 0
	v_cvt_pk_bf16_f32 v175, v171, 0
	v_cvt_pk_bf16_f32 v181, v173, 0
	v_lshlrev_b32_e32 v175, 16, v175
	v_cvt_pk_bf16_f32 v179, v172, 0
	v_lshlrev_b32_e32 v181, 16, v181
	v_sub_f32_e32 v177, v171, v175
	v_lshlrev_b32_e32 v180, 16, v179
	v_and_or_b32 v174, v174, s35, v175
	v_and_or_b32 v175, v179, s35, v181
	v_mov_b32_e32 v179, v1
	v_cvt_pk_fp8_f32 v179, v170, v171
	s_add_u32 s12, s20, s12
	s_addc_u32 s13, s21, s13
	v_sub_f32_e32 v180, v172, v180
	v_cvt_pk_fp8_f32 v179, v172, v173 op_sel:[0,0,1]
	v_sub_f32_e32 v182, v173, v181
	v_lshl_add_u64 v[172:173], s[12:13], 0, v[0:1]
	v_cvt_pk_bf16_f32 v177, v177, 0
	v_pk_mul_f32 v[166:167], v[166:167], v[178:179] op_sel_hi:[1,0]
	global_store_dword v[172:173], v179, off
	v_pk_fma_f32 v[166:167], v[14:15], v[166:167], v[22:23]
	v_pk_mul_f32 v[168:169], v[168:169], v[178:179] op_sel_hi:[1,0]
	v_pk_fma_f32 v[166:167], v[150:151], v[166:167], v[146:147]
	v_mov_b32_e32 v179, v1
	v_cvt_pk_bf16_f32 v182, v182, 0
	v_lshlrev_b32_e32 v177, 16, v177
	v_cvt_pk_fp8_f32 v179, v166, v167
	v_cvt_pk_bf16_f32 v180, v180, 0
	v_and_or_b32 v170, v176, s35, v177
	v_lshlrev_b32_e32 v171, 16, v182
	v_add_u32_e32 v172, s48, v235
	v_and_or_b32 v171, v180, s35, v171
	ds_write_b64 v172, v[174:175]
	ds_write_b64 v172, v[170:171] offset:33024
	v_pk_fma_f32 v[168:169], v[16:17], v[168:169], v[24:25]
	v_cvt_pk_bf16_f32 v170, v166, 0
	v_pk_fma_f32 v[168:169], v[152:153], v[168:169], v[148:149]
	v_lshlrev_b32_e32 v171, 16, v170
	v_sub_f32_e32 v171, v166, v171
	v_cvt_pk_fp8_f32 v179, v168, v169 op_sel:[0,0,1]
	v_cvt_pk_bf16_f32 v172, v171, 0
	v_cvt_pk_bf16_f32 v171, v167, 0
	v_lshlrev_b32_e32 v171, 16, v171
	v_cvt_pk_bf16_f32 v176, v169, 0
	v_sub_f32_e32 v173, v167, v171
	v_cvt_pk_bf16_f32 v174, v168, 0
	v_lshlrev_b32_e32 v176, 16, v176
	v_cvt_pk_bf16_f32 v173, v173, 0
	v_lshlrev_b32_e32 v175, 16, v174
	v_sub_f32_e32 v177, v169, v176
	v_pk_mul_f32 v[162:163], v[162:163], v[178:179] op_sel_hi:[1,0]
	v_sub_f32_e32 v175, v168, v175
	v_cvt_pk_bf16_f32 v177, v177, 0
	v_lshlrev_b32_e32 v166, 16, v173
	v_lshl_add_u64 v[168:169], s[12:13], 0, v[198:199]
	v_pk_fma_f32 v[162:163], v[26:27], v[162:163], v[30:31]
	v_cvt_pk_bf16_f32 v175, v175, 0
	v_and_or_b32 v170, v170, s35, v171
	v_and_or_b32 v171, v174, s35, v176
	v_and_or_b32 v166, v172, s35, v166
	v_lshlrev_b32_e32 v167, 16, v177
	global_store_dword v[168:169], v179, off
	v_add_u32_e32 v168, s48, v236
	v_pk_fma_f32 v[162:163], v[154:155], v[162:163], v[158:159]
	v_mov_b32_e32 v174, v1
	v_and_or_b32 v167, v175, s35, v167
	ds_write_b64 v168, v[170:171]
	ds_write_b64 v168, v[166:167] offset:33024
	v_pk_mul_f32 v[164:165], v[164:165], v[178:179] op_sel_hi:[1,0]
	v_cvt_pk_bf16_f32 v166, v162, 0
	v_cvt_pk_fp8_f32 v174, v162, v163
	v_pk_fma_f32 v[164:165], v[28:29], v[164:165], v[32:33]
	v_lshlrev_b32_e32 v167, 16, v166
	v_pk_fma_f32 v[164:165], v[156:157], v[164:165], v[160:161]
	v_sub_f32_e32 v167, v162, v167
	v_cvt_pk_bf16_f32 v168, v167, 0
	v_cvt_pk_bf16_f32 v167, v163, 0
	v_cvt_pk_bf16_f32 v172, v165, 0
	v_lshlrev_b32_e32 v167, 16, v167
	v_cvt_pk_bf16_f32 v170, v164, 0
	v_lshlrev_b32_e32 v172, 16, v172
	v_cvt_pk_fp8_f32 v174, v164, v165 op_sel:[0,0,1]
	v_sub_f32_e32 v169, v163, v167
	v_lshlrev_b32_e32 v171, 16, v170
	v_sub_f32_e32 v173, v165, v172
	v_cvt_pk_bf16_f32 v169, v169, 0
	v_sub_f32_e32 v171, v164, v171
	v_cvt_pk_bf16_f32 v173, v173, 0
	v_cvt_pk_bf16_f32 v171, v171, 0
	v_lshlrev_b32_e32 v162, 16, v169
	v_lshlrev_b32_e32 v163, 16, v173
	v_lshl_add_u64 v[164:165], s[12:13], 0, v[200:201]
	v_and_or_b32 v166, v166, s35, v167
	v_and_or_b32 v167, v170, s35, v172
	v_and_or_b32 v162, v168, s35, v162
	v_and_or_b32 v163, v171, s35, v163
	global_store_dword v[164:165], v174, off
	v_add_u32_e32 v164, s48, v237
	ds_write_b64 v164, v[166:167]
	ds_write_b64 v164, v[162:163] offset:33024
	s_waitcnt lgkmcnt(0)
	s_barrier
	ds_read_b128 v[162:165], v238
	ds_read_b128 v[166:169], v238 offset:64
	s_waitcnt lgkmcnt(1)
	v_mfma_f32_16x16x32_bf16 v[170:173], v[162:165], v[34:37], 0
	ds_read_b128 v[174:177], v238 offset:33024
	ds_read_b128 v[178:181], v238 offset:33088
	s_mov_b64 s[34:35], -1
	s_mov_b64 s[12:13], -1
	v_mfma_f32_16x16x32_bf16 v[182:185], v[162:165], v[42:45], 0
	s_waitcnt lgkmcnt(1)
	v_mfma_f32_16x16x32_bf16 v[170:173], v[174:177], v[34:37], v[170:173]
	v_mfma_f32_16x16x32_bf16 v[174:177], v[174:177], v[42:45], v[182:185]
	v_mfma_f32_16x16x32_bf16 v[170:173], v[162:165], v[38:41], v[170:173]
	v_mfma_f32_16x16x32_bf16 v[162:165], v[162:165], v[46:49], v[174:177]
	v_mfma_f32_16x16x32_bf16 v[170:173], v[166:169], v[50:53], v[170:173]
	v_mfma_f32_16x16x32_bf16 v[162:165], v[166:169], v[58:61], v[162:165]
	s_waitcnt lgkmcnt(0)
	v_mfma_f32_16x16x32_bf16 v[170:173], v[178:181], v[50:53], v[170:173]
	v_mfma_f32_16x16x32_bf16 v[162:165], v[178:181], v[58:61], v[162:165]
	v_mfma_f32_16x16x32_bf16 v[170:173], v[166:169], v[54:57], v[170:173]
	v_mfma_f32_16x16x32_bf16 v[162:165], v[166:169], v[62:65], v[162:165]
	ds_read_b128 v[166:169], v238 offset:128
	ds_read_b128 v[174:177], v238 offset:192
	ds_read_b128 v[178:181], v238 offset:33152
	ds_read_b128 v[182:185], v238 offset:33216
	s_waitcnt lgkmcnt(3)
	v_mfma_f32_16x16x32_bf16 v[170:173], v[166:169], v[66:69], v[170:173]
	v_mfma_f32_16x16x32_bf16 v[162:165], v[166:169], v[74:77], v[162:165]
	s_waitcnt lgkmcnt(1)
	v_mfma_f32_16x16x32_bf16 v[170:173], v[178:181], v[66:69], v[170:173]
	v_mfma_f32_16x16x32_bf16 v[162:165], v[178:181], v[74:77], v[162:165]
	v_mfma_f32_16x16x32_bf16 v[170:173], v[166:169], v[70:73], v[170:173]
	v_mfma_f32_16x16x32_bf16 v[162:165], v[166:169], v[78:81], v[162:165]
	v_mfma_f32_16x16x32_bf16 v[166:169], v[174:177], v[82:85], v[170:173]
	v_mfma_f32_16x16x32_bf16 v[162:165], v[174:177], v[90:93], v[162:165]
	s_waitcnt lgkmcnt(0)
	v_mfma_f32_16x16x32_bf16 v[166:169], v[182:185], v[82:85], v[166:169]
	v_mfma_f32_16x16x32_bf16 v[162:165], v[182:185], v[90:93], v[162:165]
	v_mfma_f32_16x16x32_bf16 v[166:169], v[174:177], v[86:89], v[166:169]
	v_mfma_f32_16x16x32_bf16 v[162:165], v[174:177], v[94:97], v[162:165]
	s_nop 7
	ds_write2_b32 v239, v166, v162 offset1:16
	ds_write2_b32 v239, v167, v163 offset0:32 offset1:48
	ds_write2_b32 v239, v168, v164 offset0:64 offset1:80
	ds_write2_b32 v239, v169, v165 offset0:96 offset1:112
	s_waitcnt lgkmcnt(0)
	s_barrier
	ds_read2st64_b32 v[162:163], v233 offset1:8
	ds_read2st64_b32 v[164:165], v233 offset0:16 offset1:24
	s_waitcnt vmcnt(0) lgkmcnt(1)
	v_add_f32_e32 v162, v242, v162
	ds_read2st64_b32 v[166:167], v233 offset0:32 offset1:40
	v_add_f32_e32 v168, v162, v163
	ds_read2st64_b32 v[162:163], v233 offset0:48 offset1:56
	s_waitcnt lgkmcnt(2)
	v_add_f32_e32 v164, v168, v164
	v_add_f32_e32 v164, v164, v165
	s_waitcnt lgkmcnt(1)
	v_add_f32_e32 v164, v164, v166
	v_add_f32_e32 v164, v164, v167
	s_waitcnt lgkmcnt(0)
	v_add_f32_e32 v162, v164, v162
	v_add_f32_e32 v165, v162, v163
	ds_bpermute_b32 v162, v230, v165
	ds_bpermute_b32 v163, v230, v232
	s_waitcnt lgkmcnt(1)
	v_cmp_nlt_f32_e32 vcc, v165, v162
	s_and_saveexec_b64 s[36:37], vcc
	s_cbranch_execz .LBB0_988
	v_cmp_eq_f32_e32 vcc, v165, v162
	s_waitcnt lgkmcnt(0)
	v_cmp_lt_i32_e64 s[12:13], v163, v232
	s_and_b64 s[12:13], vcc, s[12:13]
	s_orn2_b64 s[12:13], s[12:13], exec
